# baseline (speedup 1.0000x reference)
.LBB0_60:
	s_andn2_b64 vcc, exec, s[4:5]
	s_cbranch_vccnz .LBB0_98
	s_load_dwordx2 s[4:5], s[0:1], 0x0
	s_lshl_b32 s3, s2, 12
	v_lshlrev_b32_e32 v1, 2, v0
	v_mov_b32_e32 v2, 0
	ds_write_b32 v1, v2 offset:16384
	v_or_b32_e32 v6, s3, v0
	v_or_b32_e32 v7, 0x400, v6
	v_or_b32_e32 v8, 0x800, v6
	v_or_b32_e32 v9, 0xc00, v6
	s_mov_b32 s10, 0xf423f
	v_min_u32_e32 v14, s10, v6
	v_min_u32_e32 v15, s10, v7
	v_min_u32_e32 v16, s10, v8
	v_min_u32_e32 v17, s10, v9
	v_lshlrev_b32_e32 v14, 2, v14
	v_lshlrev_b32_e32 v15, 2, v15
	v_lshlrev_b32_e32 v16, 2, v16
	v_lshlrev_b32_e32 v17, 2, v17
	s_waitcnt lgkmcnt(0)
	s_add_u32 s6, s4, 0x3d0900
	s_addc_u32 s7, s5, 0
	global_load_dword v10, v14, s[6:7] nt
	global_load_dword v2, v14, s[4:5] nt
	s_waitcnt vmcnt(0)
	global_load_dword v11, v15, s[6:7] nt
	global_load_dword v12, v16, s[6:7] nt
	global_load_dword v13, v17, s[6:7] nt
	global_load_dword v3, v15, s[4:5] nt
	global_load_dword v4, v16, s[4:5] nt
	global_load_dword v5, v17, s[4:5] nt
	s_mov_b32 s10, 0xf4240
	s_mov_b32 s11, 0x5397829d
	v_cmp_gt_u32_e64 s[12:13], s10, v6
	v_cmp_gt_u32_e64 s[14:15], s10, v7
	v_cmp_gt_u32_e64 s[16:17], s10, v8
	v_cmp_gt_u32_e64 s[18:19], s10, v9
	s_barrier
	s_waitcnt vmcnt(3)
	v_mul_hi_u32 v14, v10, s11
	v_mul_hi_u32 v15, v11, s11
	v_mul_hi_u32 v16, v12, s11
	v_mul_hi_u32 v17, v13, s11
	v_lshrrev_b32_e32 v14, 5, v14
	v_lshrrev_b32_e32 v15, 5, v15
	v_lshrrev_b32_e32 v16, 5, v16
	v_lshrrev_b32_e32 v17, 5, v17
	v_mul_u32_u24_e32 v6, 0x62, v14
	v_mul_u32_u24_e32 v7, 0x62, v15
	v_mul_u32_u24_e32 v8, 0x62, v16
	v_mul_u32_u24_e32 v9, 0x62, v17
	v_sub_u32_e32 v6, v10, v6
	v_sub_u32_e32 v7, v11, v7
	v_sub_u32_e32 v8, v12, v8
	v_sub_u32_e32 v9, v13, v9
	v_cndmask_b32_e64 v10, -1, v14, s[12:13]
	v_cndmask_b32_e64 v11, -1, v15, s[14:15]
	v_cndmask_b32_e64 v12, -1, v16, s[16:17]
	v_cndmask_b32_e64 v13, -1, v17, s[18:19]
	s_waitcnt vmcnt(0)
	v_lshl_or_b32 v2, v6, 17, v2
	v_lshl_or_b32 v3, v7, 17, v3
	v_lshl_or_b32 v4, v8, 17, v4
	v_lshl_or_b32 v5, v9, 17, v5
	v_mov_b32_e32 v6, 0
	v_mov_b32_e32 v7, 0
	v_mov_b32_e32 v8, 0
	v_mov_b32_e32 v9, 0
	v_mov_b32_e32 v15, 1
	v_cmp_lt_i32_e32 vcc, -1, v10
	v_cmp_lt_i32_e64 s[8:9], -1, v11
	v_cmp_lt_i32_e64 s[4:5], -1, v12
	v_cmp_lt_i32_e64 s[6:7], -1, v13
	v_lshlrev_b32_e32 v10, 2, v10
	v_lshlrev_b32_e32 v11, 2, v11
	v_lshlrev_b32_e32 v12, 2, v12
	v_lshlrev_b32_e32 v13, 2, v13
	v_or_b32_e32 v14, 0x4000, v1
	s_mov_b64 s[10:11], exec
	s_and_b64 exec, s[10:11], vcc
	ds_add_rtn_u32 v6, v10, v15 offset:16384
	s_and_b64 exec, s[10:11], s[8:9]
	ds_add_rtn_u32 v7, v11, v15 offset:16384
	s_and_b64 exec, s[10:11], s[4:5]
	ds_add_rtn_u32 v8, v12, v15 offset:16384
	s_and_b64 exec, s[10:11], s[6:7]
	ds_add_rtn_u32 v9, v13, v15 offset:16384
	s_or_b64 exec, exec, s[10:11]
	s_waitcnt lgkmcnt(0)
	s_barrier
	ds_read_b32 v15, v14
	v_and_b32_e32 v18, 63, v0
	v_mov_b32_e32 v17, 0
	v_cmp_eq_u32_e64 s[10:11], 63, v18
	v_lshrrev_b32_e32 v19, 6, v0
	s_waitcnt lgkmcnt(0)
	v_add_u32_dpp v16, v15, v15 row_shr:1 row_mask:0xf bank_mask:0xf bound_ctrl:1
	s_nop 1
	v_add_u32_dpp v16, v16, v16 row_shr:2 row_mask:0xf bank_mask:0xf bound_ctrl:1
	s_nop 1
	v_add_u32_dpp v16, v16, v16 row_shr:4 row_mask:0xf bank_mask:0xf bound_ctrl:1
	s_nop 1
	v_add_u32_dpp v16, v16, v16 row_shr:8 row_mask:0xf bank_mask:0xf bound_ctrl:1
	s_nop 1
	v_add_u32_dpp v16, v16, v16 row_bcast:15 row_mask:0xa bank_mask:0xf
	s_nop 1
	v_add_u32_dpp v16, v16, v16 row_bcast:31 row_mask:0xc bank_mask:0xf
	s_and_saveexec_b64 s[12:13], s[10:11]
	v_lshlrev_b32_e32 v18, 2, v19
	ds_write_b32 v18, v16 offset:20480
	s_or_b64 exec, exec, s[12:13]
	s_load_dwordx4 s[12:15], s[0:1], 0x30
	v_cmp_lt_u32_e64 s[0:1], 63, v0
	s_waitcnt lgkmcnt(0)
	s_barrier
	s_and_saveexec_b64 s[10:11], s[0:1]
	s_cbranch_execz .LBB0_89
	v_add_u32_e32 v17, -1, v19
	v_cmp_lt_u32_e64 s[0:1], 6, v17
	v_mov_b32_e32 v18, 0
	v_mov_b32_e32 v17, 0
	s_and_saveexec_b64 s[16:17], s[0:1]
	s_cbranch_execz .LBB0_84
	v_and_b32_e32 v18, 8, v19
	s_mov_b32 s20, 0
	s_movk_i32 s21, 0x5000
	s_mov_b64 s[18:19], 0
	v_mov_b32_e32 v17, 0
